# P0 modulation GEMV: weight loads software-pipelined (two 32-load groups in flight)
# speedup vs baseline: 1.0096x; 1.0058x over previous
.LBB0_14:
	s_or_b64 exec, exec, s[0:1]
	s_cmpk_gt_i32 s18, 0xbf
	s_waitcnt lgkmcnt(0)
	s_barrier
	s_cbranch_scc1 .LBB0_22
	v_ashrrev_i32_e32 v4, 7, v6
	v_lshlrev_b32_e32 v2, 8, v4
	s_add_i32 s8, 0, 0x1a000
	s_movk_i32 s2, 0x1200
	s_movk_i32 s12, 0x6000
	v_and_b32_e32 v1, 0x7f, v6
	s_add_u32 s4, s6, 0x200000
	v_mul_lo_u32 v5, v4, s2
	v_mad_i64_i32 v[2:3], s[2:3], v2, s12, 0
	v_lshl_add_u32 v18, v1, 2, s8
	s_movk_i32 s0, 0x480
	s_addc_u32 s5, s7, 0
	s_add_i32 s2, 0, 0x25d20
	v_cmp_gt_i32_e64 s[0:1], s0, v6
	v_lshl_add_u32 v19, v4, 10, 0
	v_lshl_add_u32 v20, v6, 2, s8
	v_mov_b32_e32 v21, s2
	v_mov_b32_e32 v22, 0x1800000
	s_mov_b32 s13, 0xffff4000
	s_movk_i32 s14, 0xa000
	s_mov_b64 s[8:9], 0x6000
	v_add_u32_e32 v23, v18, v5
	s_add_i32 s15, 0, 0x25d28
	s_movk_i32 s19, 0x27f
	s_mov_b32 s20, s18
	s_branch .LBB0_17

.LBB0_17:
	s_mul_hi_i32 s2, s20, 0x2aaaaaab
	s_lshr_b32 s3, s2, 31
	s_ashr_i32 s10, s2, 3
	ds_read_b64 v[8:9], v21
	s_add_i32 s10, s10, s3
	s_mul_i32 s2, s10, 48
	s_sub_i32 s2, s20, s2
	v_lshl_or_b32 v4, s2, 7, v1
	v_ashrrev_i32_e32 v5, 31, v4
	s_waitcnt lgkmcnt(0)
	v_readfirstlane_b32 s2, v8
	v_readfirstlane_b32 s3, v9
	v_lshlrev_b64 v[10:11], 2, v[4:5]
	v_mov_b32_e32 v24, 0
	v_lshl_add_u64 v[8:9], s[2:3], 0, v[2:3]
	v_mad_i64_i32 v[10:11], s[2:3], s10, v22, v[10:11]
	v_lshl_add_u64 v[8:9], v[8:9], 0, v[10:11]
	s_mov_b32 s11, 0
	v_mov_b32_e32 v10, 0
	v_mov_b32_e32 v11, v24
	v_mov_b32_e32 v12, 0
	v_mov_b32_e32 v13, v24
	v_mov_b32_e32 v14, 0
	v_mov_b32_e32 v15, v24
	v_mov_b32_e32 v16, 0
	v_mov_b32_e32 v17, v24
	global_load_dword v72, v[8:9], off
	v_lshl_add_u64 v[8:9], v[8:9], 0, s[8:9]
	global_load_dword v74, v[8:9], off
	v_lshl_add_u64 v[8:9], v[8:9], 0, s[8:9]
	global_load_dword v76, v[8:9], off
	v_lshl_add_u64 v[8:9], v[8:9], 0, s[8:9]
	global_load_dword v78, v[8:9], off
	v_lshl_add_u64 v[8:9], v[8:9], 0, s[8:9]
	global_load_dword v80, v[8:9], off
	v_lshl_add_u64 v[8:9], v[8:9], 0, s[8:9]
	global_load_dword v82, v[8:9], off
	v_lshl_add_u64 v[8:9], v[8:9], 0, s[8:9]
	global_load_dword v84, v[8:9], off
	v_lshl_add_u64 v[8:9], v[8:9], 0, s[8:9]
	global_load_dword v86, v[8:9], off
	v_lshl_add_u64 v[8:9], v[8:9], 0, s[8:9]
	global_load_dword v88, v[8:9], off
	v_lshl_add_u64 v[8:9], v[8:9], 0, s[8:9]
	global_load_dword v90, v[8:9], off
	v_lshl_add_u64 v[8:9], v[8:9], 0, s[8:9]
	global_load_dword v92, v[8:9], off
	v_lshl_add_u64 v[8:9], v[8:9], 0, s[8:9]
	global_load_dword v94, v[8:9], off
	v_lshl_add_u64 v[8:9], v[8:9], 0, s[8:9]
	global_load_dword v96, v[8:9], off
	v_lshl_add_u64 v[8:9], v[8:9], 0, s[8:9]
	global_load_dword v98, v[8:9], off
	v_lshl_add_u64 v[8:9], v[8:9], 0, s[8:9]
	global_load_dword v100, v[8:9], off
	v_lshl_add_u64 v[8:9], v[8:9], 0, s[8:9]
	global_load_dword v102, v[8:9], off
	v_lshl_add_u64 v[8:9], v[8:9], 0, s[8:9]
	global_load_dword v104, v[8:9], off
	v_lshl_add_u64 v[8:9], v[8:9], 0, s[8:9]
	global_load_dword v106, v[8:9], off
	v_lshl_add_u64 v[8:9], v[8:9], 0, s[8:9]
	global_load_dword v108, v[8:9], off
	v_lshl_add_u64 v[8:9], v[8:9], 0, s[8:9]
	global_load_dword v110, v[8:9], off
	v_lshl_add_u64 v[8:9], v[8:9], 0, s[8:9]
	global_load_dword v112, v[8:9], off
	v_lshl_add_u64 v[8:9], v[8:9], 0, s[8:9]
	global_load_dword v114, v[8:9], off
	v_lshl_add_u64 v[8:9], v[8:9], 0, s[8:9]
	global_load_dword v116, v[8:9], off
	v_lshl_add_u64 v[8:9], v[8:9], 0, s[8:9]
	global_load_dword v118, v[8:9], off
	v_lshl_add_u64 v[8:9], v[8:9], 0, s[8:9]
	global_load_dword v120, v[8:9], off
	v_lshl_add_u64 v[8:9], v[8:9], 0, s[8:9]
	global_load_dword v122, v[8:9], off
	v_lshl_add_u64 v[8:9], v[8:9], 0, s[8:9]
	global_load_dword v124, v[8:9], off
	v_lshl_add_u64 v[8:9], v[8:9], 0, s[8:9]
	global_load_dword v126, v[8:9], off
	v_lshl_add_u64 v[8:9], v[8:9], 0, s[8:9]
	global_load_dword v128, v[8:9], off
	v_lshl_add_u64 v[8:9], v[8:9], 0, s[8:9]
	global_load_dword v130, v[8:9], off
	v_lshl_add_u64 v[8:9], v[8:9], 0, s[8:9]
	global_load_dword v132, v[8:9], off
	v_lshl_add_u64 v[8:9], v[8:9], 0, s[8:9]
	global_load_dword v134, v[8:9], off
	v_lshl_add_u64 v[8:9], v[8:9], 0, s[8:9]
	global_load_dword v136, v[8:9], off
	v_lshl_add_u64 v[8:9], v[8:9], 0, s[8:9]
	global_load_dword v138, v[8:9], off
	v_lshl_add_u64 v[8:9], v[8:9], 0, s[8:9]
	global_load_dword v140, v[8:9], off
	v_lshl_add_u64 v[8:9], v[8:9], 0, s[8:9]
	global_load_dword v142, v[8:9], off
	v_lshl_add_u64 v[8:9], v[8:9], 0, s[8:9]
	global_load_dword v144, v[8:9], off
	v_lshl_add_u64 v[8:9], v[8:9], 0, s[8:9]
	global_load_dword v146, v[8:9], off
	v_lshl_add_u64 v[8:9], v[8:9], 0, s[8:9]
	global_load_dword v148, v[8:9], off
	v_lshl_add_u64 v[8:9], v[8:9], 0, s[8:9]
	global_load_dword v150, v[8:9], off
	v_lshl_add_u64 v[8:9], v[8:9], 0, s[8:9]
	global_load_dword v152, v[8:9], off
	v_lshl_add_u64 v[8:9], v[8:9], 0, s[8:9]
	global_load_dword v154, v[8:9], off
	v_lshl_add_u64 v[8:9], v[8:9], 0, s[8:9]
	global_load_dword v156, v[8:9], off
	v_lshl_add_u64 v[8:9], v[8:9], 0, s[8:9]
	global_load_dword v158, v[8:9], off
	v_lshl_add_u64 v[8:9], v[8:9], 0, s[8:9]
	global_load_dword v160, v[8:9], off
	v_lshl_add_u64 v[8:9], v[8:9], 0, s[8:9]
	global_load_dword v162, v[8:9], off
	v_lshl_add_u64 v[8:9], v[8:9], 0, s[8:9]
	global_load_dword v164, v[8:9], off
	v_lshl_add_u64 v[8:9], v[8:9], 0, s[8:9]
	global_load_dword v166, v[8:9], off
	v_lshl_add_u64 v[8:9], v[8:9], 0, s[8:9]
	global_load_dword v168, v[8:9], off
	v_lshl_add_u64 v[8:9], v[8:9], 0, s[8:9]
	global_load_dword v170, v[8:9], off
	v_lshl_add_u64 v[8:9], v[8:9], 0, s[8:9]
	global_load_dword v172, v[8:9], off
	v_lshl_add_u64 v[8:9], v[8:9], 0, s[8:9]
	global_load_dword v174, v[8:9], off
	v_lshl_add_u64 v[8:9], v[8:9], 0, s[8:9]
	global_load_dword v176, v[8:9], off
	v_lshl_add_u64 v[8:9], v[8:9], 0, s[8:9]
	global_load_dword v178, v[8:9], off
	v_lshl_add_u64 v[8:9], v[8:9], 0, s[8:9]
	global_load_dword v180, v[8:9], off
	v_lshl_add_u64 v[8:9], v[8:9], 0, s[8:9]
	global_load_dword v182, v[8:9], off
	v_lshl_add_u64 v[8:9], v[8:9], 0, s[8:9]
	global_load_dword v184, v[8:9], off
	v_lshl_add_u64 v[8:9], v[8:9], 0, s[8:9]
	global_load_dword v186, v[8:9], off
	v_lshl_add_u64 v[8:9], v[8:9], 0, s[8:9]
	global_load_dword v188, v[8:9], off
	v_lshl_add_u64 v[8:9], v[8:9], 0, s[8:9]
	global_load_dword v190, v[8:9], off
	v_lshl_add_u64 v[8:9], v[8:9], 0, s[8:9]
	global_load_dword v192, v[8:9], off
	v_lshl_add_u64 v[8:9], v[8:9], 0, s[8:9]
	global_load_dword v194, v[8:9], off
	v_lshl_add_u64 v[8:9], v[8:9], 0, s[8:9]
	global_load_dword v196, v[8:9], off
	v_lshl_add_u64 v[8:9], v[8:9], 0, s[8:9]
	global_load_dword v198, v[8:9], off
	v_lshl_add_u64 v[8:9], v[8:9], 0, s[8:9]
.Lmod_loop:
	v_add_u32_e32 v25, s11, v19
	v_add_u32_e32 v26, 0x11000, v25
	v_add_u32_e32 v30, 0x12000, v25
	v_add_u32_e32 v34, 0x13000, v25
	v_add_u32_e32 v38, 0x14000, v25
	v_add_u32_e32 v42, 0x15000, v25
	v_add_u32_e32 v46, 0x16000, v25
	v_add_u32_e32 v50, 0x17000, v25
	v_add_u32_e32 v54, 0x18000, v25
	v_add_u32_e32 v25, 0x19000, v25
	ds_read_b128 v[26:29], v26
	ds_read_b128 v[30:33], v30
	ds_read_b128 v[34:37], v34
	ds_read_b128 v[38:41], v38
	ds_read_b128 v[42:45], v42
	ds_read_b128 v[46:49], v46
	ds_read_b128 v[50:53], v50
	ds_read_b128 v[54:57], v54
	ds_read_b128 v[58:61], v25
	s_waitcnt lgkmcnt(8)
	v_mov_b32_e32 v70, v26
	s_waitcnt lgkmcnt(7)
	v_mov_b32_e32 v71, v30
	v_mov_b32_e32 v30, v27
	v_mov_b32_e32 v26, v28
	v_mov_b32_e32 v27, v32
	v_mov_b32_e32 v32, v29
	s_waitcnt lgkmcnt(6)
	v_mov_b32_e32 v28, v34
	s_waitcnt lgkmcnt(5)
	v_mov_b32_e32 v29, v38
	v_mov_b32_e32 v38, v35
	v_mov_b32_e32 v34, v36
	v_mov_b32_e32 v35, v40
	v_mov_b32_e32 v40, v37
	s_waitcnt lgkmcnt(4)
	v_mov_b32_e32 v36, v42
	s_waitcnt lgkmcnt(3)
	v_mov_b32_e32 v37, v46
	v_mov_b32_e32 v46, v43
	v_mov_b32_e32 v42, v44
	v_mov_b32_e32 v43, v48
	v_mov_b32_e32 v48, v45
	s_waitcnt lgkmcnt(2)
	v_mov_b32_e32 v44, v50
	s_waitcnt lgkmcnt(1)
	v_mov_b32_e32 v45, v54
	v_mov_b32_e32 v54, v51
	v_mov_b32_e32 v50, v52
	v_mov_b32_e32 v51, v56
	v_mov_b32_e32 v56, v53
	s_waitcnt vmcnt(60)
	v_pk_fma_f32 v[10:11], v[72:73], v[70:71], v[10:11] op_sel_hi:[0,1,1]
	v_pk_fma_f32 v[12:13], v[72:73], v[28:29], v[12:13] op_sel_hi:[0,1,1]
	v_pk_fma_f32 v[14:15], v[72:73], v[36:37], v[14:15] op_sel_hi:[0,1,1]
	v_pk_fma_f32 v[16:17], v[72:73], v[44:45], v[16:17] op_sel_hi:[0,1,1]
	s_waitcnt lgkmcnt(0)
	v_fmac_f32_e32 v24, v72, v58
	v_pk_fma_f32 v[10:11], v[74:75], v[30:31], v[10:11] op_sel_hi:[0,1,1]
	v_pk_fma_f32 v[12:13], v[74:75], v[38:39], v[12:13] op_sel_hi:[0,1,1]
	v_pk_fma_f32 v[14:15], v[74:75], v[46:47], v[14:15] op_sel_hi:[0,1,1]
	v_pk_fma_f32 v[16:17], v[74:75], v[54:55], v[16:17] op_sel_hi:[0,1,1]
	v_fmac_f32_e32 v24, v74, v59
	v_pk_fma_f32 v[10:11], v[76:77], v[26:27], v[10:11] op_sel_hi:[0,1,1]
	v_pk_fma_f32 v[12:13], v[76:77], v[34:35], v[12:13] op_sel_hi:[0,1,1]
	v_pk_fma_f32 v[14:15], v[76:77], v[42:43], v[14:15] op_sel_hi:[0,1,1]
	v_pk_fma_f32 v[16:17], v[76:77], v[50:51], v[16:17] op_sel_hi:[0,1,1]
	v_fmac_f32_e32 v24, v76, v60
	v_pk_fma_f32 v[10:11], v[78:79], v[32:33], v[10:11] op_sel_hi:[0,1,1]
	v_pk_fma_f32 v[12:13], v[78:79], v[40:41], v[12:13] op_sel_hi:[0,1,1]
	v_pk_fma_f32 v[14:15], v[78:79], v[48:49], v[14:15] op_sel_hi:[0,1,1]
	v_pk_fma_f32 v[16:17], v[78:79], v[56:57], v[16:17] op_sel_hi:[0,1,1]
	v_fmac_f32_e32 v24, v78, v61
	v_add_u32_e32 v25, s11, v19
	v_add_u32_e32 v26, 0x11000, v25
	v_add_u32_e32 v30, 0x12000, v25
	v_add_u32_e32 v34, 0x13000, v25
	v_add_u32_e32 v38, 0x14000, v25
	v_add_u32_e32 v42, 0x15000, v25
	v_add_u32_e32 v46, 0x16000, v25
	v_add_u32_e32 v50, 0x17000, v25
	v_add_u32_e32 v54, 0x18000, v25
	v_add_u32_e32 v25, 0x19000, v25
	ds_read_b128 v[26:29], v26 offset:16
	ds_read_b128 v[30:33], v30 offset:16
	ds_read_b128 v[34:37], v34 offset:16
	ds_read_b128 v[38:41], v38 offset:16
	ds_read_b128 v[42:45], v42 offset:16
	ds_read_b128 v[46:49], v46 offset:16
	ds_read_b128 v[50:53], v50 offset:16
	ds_read_b128 v[54:57], v54 offset:16
	ds_read_b128 v[58:61], v25 offset:16
	s_waitcnt lgkmcnt(8)
	v_mov_b32_e32 v70, v26
	s_waitcnt lgkmcnt(7)
	v_mov_b32_e32 v71, v30
	v_mov_b32_e32 v30, v27
	v_mov_b32_e32 v26, v28
	v_mov_b32_e32 v27, v32
	v_mov_b32_e32 v32, v29
	s_waitcnt lgkmcnt(6)
	v_mov_b32_e32 v28, v34
	s_waitcnt lgkmcnt(5)
	v_mov_b32_e32 v29, v38
	v_mov_b32_e32 v38, v35
	v_mov_b32_e32 v34, v36
	v_mov_b32_e32 v35, v40
	v_mov_b32_e32 v40, v37
	s_waitcnt lgkmcnt(4)
	v_mov_b32_e32 v36, v42
	s_waitcnt lgkmcnt(3)
	v_mov_b32_e32 v37, v46
	v_mov_b32_e32 v46, v43
	v_mov_b32_e32 v42, v44
	v_mov_b32_e32 v43, v48
	v_mov_b32_e32 v48, v45
	s_waitcnt lgkmcnt(2)
	v_mov_b32_e32 v44, v50
	s_waitcnt lgkmcnt(1)
	v_mov_b32_e32 v45, v54
	v_mov_b32_e32 v54, v51
	v_mov_b32_e32 v50, v52
	v_mov_b32_e32 v51, v56
	v_mov_b32_e32 v56, v53
	s_waitcnt vmcnt(56)
	v_pk_fma_f32 v[10:11], v[80:81], v[70:71], v[10:11] op_sel_hi:[0,1,1]
	v_pk_fma_f32 v[12:13], v[80:81], v[28:29], v[12:13] op_sel_hi:[0,1,1]
	v_pk_fma_f32 v[14:15], v[80:81], v[36:37], v[14:15] op_sel_hi:[0,1,1]
	v_pk_fma_f32 v[16:17], v[80:81], v[44:45], v[16:17] op_sel_hi:[0,1,1]
	s_waitcnt lgkmcnt(0)
	v_fmac_f32_e32 v24, v80, v58
	v_pk_fma_f32 v[10:11], v[82:83], v[30:31], v[10:11] op_sel_hi:[0,1,1]
	v_pk_fma_f32 v[12:13], v[82:83], v[38:39], v[12:13] op_sel_hi:[0,1,1]
	v_pk_fma_f32 v[14:15], v[82:83], v[46:47], v[14:15] op_sel_hi:[0,1,1]
	v_pk_fma_f32 v[16:17], v[82:83], v[54:55], v[16:17] op_sel_hi:[0,1,1]
	v_fmac_f32_e32 v24, v82, v59
	v_pk_fma_f32 v[10:11], v[84:85], v[26:27], v[10:11] op_sel_hi:[0,1,1]
	v_pk_fma_f32 v[12:13], v[84:85], v[34:35], v[12:13] op_sel_hi:[0,1,1]
	v_pk_fma_f32 v[14:15], v[84:85], v[42:43], v[14:15] op_sel_hi:[0,1,1]
	v_pk_fma_f32 v[16:17], v[84:85], v[50:51], v[16:17] op_sel_hi:[0,1,1]
	v_fmac_f32_e32 v24, v84, v60
	v_pk_fma_f32 v[10:11], v[86:87], v[32:33], v[10:11] op_sel_hi:[0,1,1]
	v_pk_fma_f32 v[12:13], v[86:87], v[40:41], v[12:13] op_sel_hi:[0,1,1]
	v_pk_fma_f32 v[14:15], v[86:87], v[48:49], v[14:15] op_sel_hi:[0,1,1]
	v_pk_fma_f32 v[16:17], v[86:87], v[56:57], v[16:17] op_sel_hi:[0,1,1]
	v_fmac_f32_e32 v24, v86, v61
	v_add_u32_e32 v25, s11, v19
	v_add_u32_e32 v26, 0x11000, v25
	v_add_u32_e32 v30, 0x12000, v25
	v_add_u32_e32 v34, 0x13000, v25
	v_add_u32_e32 v38, 0x14000, v25
	v_add_u32_e32 v42, 0x15000, v25
	v_add_u32_e32 v46, 0x16000, v25
	v_add_u32_e32 v50, 0x17000, v25
	v_add_u32_e32 v54, 0x18000, v25
	v_add_u32_e32 v25, 0x19000, v25
	ds_read_b128 v[26:29], v26 offset:32
	ds_read_b128 v[30:33], v30 offset:32
	ds_read_b128 v[34:37], v34 offset:32
	ds_read_b128 v[38:41], v38 offset:32
	ds_read_b128 v[42:45], v42 offset:32
	ds_read_b128 v[46:49], v46 offset:32
	ds_read_b128 v[50:53], v50 offset:32
	ds_read_b128 v[54:57], v54 offset:32
	ds_read_b128 v[58:61], v25 offset:32
	s_waitcnt lgkmcnt(8)
	v_mov_b32_e32 v70, v26
	s_waitcnt lgkmcnt(7)
	v_mov_b32_e32 v71, v30
	v_mov_b32_e32 v30, v27
	v_mov_b32_e32 v26, v28
	v_mov_b32_e32 v27, v32
	v_mov_b32_e32 v32, v29
	s_waitcnt lgkmcnt(6)
	v_mov_b32_e32 v28, v34
	s_waitcnt lgkmcnt(5)
	v_mov_b32_e32 v29, v38
	v_mov_b32_e32 v38, v35
	v_mov_b32_e32 v34, v36
	v_mov_b32_e32 v35, v40
	v_mov_b32_e32 v40, v37
	s_waitcnt lgkmcnt(4)
	v_mov_b32_e32 v36, v42
	s_waitcnt lgkmcnt(3)
	v_mov_b32_e32 v37, v46
	v_mov_b32_e32 v46, v43
	v_mov_b32_e32 v42, v44
	v_mov_b32_e32 v43, v48
	v_mov_b32_e32 v48, v45
	s_waitcnt lgkmcnt(2)
	v_mov_b32_e32 v44, v50
	s_waitcnt lgkmcnt(1)
	v_mov_b32_e32 v45, v54
	v_mov_b32_e32 v54, v51
	v_mov_b32_e32 v50, v52
	v_mov_b32_e32 v51, v56
	v_mov_b32_e32 v56, v53
	s_waitcnt vmcnt(52)
	v_pk_fma_f32 v[10:11], v[88:89], v[70:71], v[10:11] op_sel_hi:[0,1,1]
	v_pk_fma_f32 v[12:13], v[88:89], v[28:29], v[12:13] op_sel_hi:[0,1,1]
	v_pk_fma_f32 v[14:15], v[88:89], v[36:37], v[14:15] op_sel_hi:[0,1,1]
	v_pk_fma_f32 v[16:17], v[88:89], v[44:45], v[16:17] op_sel_hi:[0,1,1]
	s_waitcnt lgkmcnt(0)
	v_fmac_f32_e32 v24, v88, v58
	v_pk_fma_f32 v[10:11], v[90:91], v[30:31], v[10:11] op_sel_hi:[0,1,1]
	v_pk_fma_f32 v[12:13], v[90:91], v[38:39], v[12:13] op_sel_hi:[0,1,1]
	v_pk_fma_f32 v[14:15], v[90:91], v[46:47], v[14:15] op_sel_hi:[0,1,1]
	v_pk_fma_f32 v[16:17], v[90:91], v[54:55], v[16:17] op_sel_hi:[0,1,1]
	v_fmac_f32_e32 v24, v90, v59
	v_pk_fma_f32 v[10:11], v[92:93], v[26:27], v[10:11] op_sel_hi:[0,1,1]
	v_pk_fma_f32 v[12:13], v[92:93], v[34:35], v[12:13] op_sel_hi:[0,1,1]
	v_pk_fma_f32 v[14:15], v[92:93], v[42:43], v[14:15] op_sel_hi:[0,1,1]
	v_pk_fma_f32 v[16:17], v[92:93], v[50:51], v[16:17] op_sel_hi:[0,1,1]
	v_fmac_f32_e32 v24, v92, v60
	v_pk_fma_f32 v[10:11], v[94:95], v[32:33], v[10:11] op_sel_hi:[0,1,1]
	v_pk_fma_f32 v[12:13], v[94:95], v[40:41], v[12:13] op_sel_hi:[0,1,1]
	v_pk_fma_f32 v[14:15], v[94:95], v[48:49], v[14:15] op_sel_hi:[0,1,1]
	v_pk_fma_f32 v[16:17], v[94:95], v[56:57], v[16:17] op_sel_hi:[0,1,1]
	v_fmac_f32_e32 v24, v94, v61
	v_add_u32_e32 v25, s11, v19
	v_add_u32_e32 v26, 0x11000, v25
	v_add_u32_e32 v30, 0x12000, v25
	v_add_u32_e32 v34, 0x13000, v25
	v_add_u32_e32 v38, 0x14000, v25
	v_add_u32_e32 v42, 0x15000, v25
	v_add_u32_e32 v46, 0x16000, v25
	v_add_u32_e32 v50, 0x17000, v25
	v_add_u32_e32 v54, 0x18000, v25
	v_add_u32_e32 v25, 0x19000, v25
	ds_read_b128 v[26:29], v26 offset:48
	ds_read_b128 v[30:33], v30 offset:48
	ds_read_b128 v[34:37], v34 offset:48
	ds_read_b128 v[38:41], v38 offset:48
	ds_read_b128 v[42:45], v42 offset:48
	ds_read_b128 v[46:49], v46 offset:48
	ds_read_b128 v[50:53], v50 offset:48
	ds_read_b128 v[54:57], v54 offset:48
	ds_read_b128 v[58:61], v25 offset:48
	s_waitcnt lgkmcnt(8)
	v_mov_b32_e32 v70, v26
	s_waitcnt lgkmcnt(7)
	v_mov_b32_e32 v71, v30
	v_mov_b32_e32 v30, v27
	v_mov_b32_e32 v26, v28
	v_mov_b32_e32 v27, v32
	v_mov_b32_e32 v32, v29
	s_waitcnt lgkmcnt(6)
	v_mov_b32_e32 v28, v34
	s_waitcnt lgkmcnt(5)
	v_mov_b32_e32 v29, v38
	v_mov_b32_e32 v38, v35
	v_mov_b32_e32 v34, v36
	v_mov_b32_e32 v35, v40
	v_mov_b32_e32 v40, v37
	s_waitcnt lgkmcnt(4)
	v_mov_b32_e32 v36, v42
	s_waitcnt lgkmcnt(3)
	v_mov_b32_e32 v37, v46
	v_mov_b32_e32 v46, v43
	v_mov_b32_e32 v42, v44
	v_mov_b32_e32 v43, v48
	v_mov_b32_e32 v48, v45
	s_waitcnt lgkmcnt(2)
	v_mov_b32_e32 v44, v50
	s_waitcnt lgkmcnt(1)
	v_mov_b32_e32 v45, v54
	v_mov_b32_e32 v54, v51
	v_mov_b32_e32 v50, v52
	v_mov_b32_e32 v51, v56
	v_mov_b32_e32 v56, v53
	s_waitcnt vmcnt(48)
	v_pk_fma_f32 v[10:11], v[96:97], v[70:71], v[10:11] op_sel_hi:[0,1,1]
	v_pk_fma_f32 v[12:13], v[96:97], v[28:29], v[12:13] op_sel_hi:[0,1,1]
	v_pk_fma_f32 v[14:15], v[96:97], v[36:37], v[14:15] op_sel_hi:[0,1,1]
	v_pk_fma_f32 v[16:17], v[96:97], v[44:45], v[16:17] op_sel_hi:[0,1,1]
	s_waitcnt lgkmcnt(0)
	v_fmac_f32_e32 v24, v96, v58
	v_pk_fma_f32 v[10:11], v[98:99], v[30:31], v[10:11] op_sel_hi:[0,1,1]
	v_pk_fma_f32 v[12:13], v[98:99], v[38:39], v[12:13] op_sel_hi:[0,1,1]
	v_pk_fma_f32 v[14:15], v[98:99], v[46:47], v[14:15] op_sel_hi:[0,1,1]
	v_pk_fma_f32 v[16:17], v[98:99], v[54:55], v[16:17] op_sel_hi:[0,1,1]
	v_fmac_f32_e32 v24, v98, v59
	v_pk_fma_f32 v[10:11], v[100:101], v[26:27], v[10:11] op_sel_hi:[0,1,1]
	v_pk_fma_f32 v[12:13], v[100:101], v[34:35], v[12:13] op_sel_hi:[0,1,1]
	v_pk_fma_f32 v[14:15], v[100:101], v[42:43], v[14:15] op_sel_hi:[0,1,1]
	v_pk_fma_f32 v[16:17], v[100:101], v[50:51], v[16:17] op_sel_hi:[0,1,1]
	v_fmac_f32_e32 v24, v100, v60
	v_pk_fma_f32 v[10:11], v[102:103], v[32:33], v[10:11] op_sel_hi:[0,1,1]
	v_pk_fma_f32 v[12:13], v[102:103], v[40:41], v[12:13] op_sel_hi:[0,1,1]
	v_pk_fma_f32 v[14:15], v[102:103], v[48:49], v[14:15] op_sel_hi:[0,1,1]
	v_pk_fma_f32 v[16:17], v[102:103], v[56:57], v[16:17] op_sel_hi:[0,1,1]
	v_fmac_f32_e32 v24, v102, v61
	v_add_u32_e32 v25, s11, v19
	v_add_u32_e32 v26, 0x11000, v25
	v_add_u32_e32 v30, 0x12000, v25
	v_add_u32_e32 v34, 0x13000, v25
	v_add_u32_e32 v38, 0x14000, v25
	v_add_u32_e32 v42, 0x15000, v25
	v_add_u32_e32 v46, 0x16000, v25
	v_add_u32_e32 v50, 0x17000, v25
	v_add_u32_e32 v54, 0x18000, v25
	v_add_u32_e32 v25, 0x19000, v25
	ds_read_b128 v[26:29], v26 offset:64
	ds_read_b128 v[30:33], v30 offset:64
	ds_read_b128 v[34:37], v34 offset:64
	ds_read_b128 v[38:41], v38 offset:64
	ds_read_b128 v[42:45], v42 offset:64
	ds_read_b128 v[46:49], v46 offset:64
	ds_read_b128 v[50:53], v50 offset:64
	ds_read_b128 v[54:57], v54 offset:64
	ds_read_b128 v[58:61], v25 offset:64
	s_waitcnt lgkmcnt(8)
	v_mov_b32_e32 v70, v26
	s_waitcnt lgkmcnt(7)
	v_mov_b32_e32 v71, v30
	v_mov_b32_e32 v30, v27
	v_mov_b32_e32 v26, v28
	v_mov_b32_e32 v27, v32
	v_mov_b32_e32 v32, v29
	s_waitcnt lgkmcnt(6)
	v_mov_b32_e32 v28, v34
	s_waitcnt lgkmcnt(5)
	v_mov_b32_e32 v29, v38
	v_mov_b32_e32 v38, v35
	v_mov_b32_e32 v34, v36
	v_mov_b32_e32 v35, v40
	v_mov_b32_e32 v40, v37
	s_waitcnt lgkmcnt(4)
	v_mov_b32_e32 v36, v42
	s_waitcnt lgkmcnt(3)
	v_mov_b32_e32 v37, v46
	v_mov_b32_e32 v46, v43
	v_mov_b32_e32 v42, v44
	v_mov_b32_e32 v43, v48
	v_mov_b32_e32 v48, v45
	s_waitcnt lgkmcnt(2)
	v_mov_b32_e32 v44, v50
	s_waitcnt lgkmcnt(1)
	v_mov_b32_e32 v45, v54
	v_mov_b32_e32 v54, v51
	v_mov_b32_e32 v50, v52
	v_mov_b32_e32 v51, v56
	v_mov_b32_e32 v56, v53
	s_waitcnt vmcnt(44)
	v_pk_fma_f32 v[10:11], v[104:105], v[70:71], v[10:11] op_sel_hi:[0,1,1]
	v_pk_fma_f32 v[12:13], v[104:105], v[28:29], v[12:13] op_sel_hi:[0,1,1]
	v_pk_fma_f32 v[14:15], v[104:105], v[36:37], v[14:15] op_sel_hi:[0,1,1]
	v_pk_fma_f32 v[16:17], v[104:105], v[44:45], v[16:17] op_sel_hi:[0,1,1]
	s_waitcnt lgkmcnt(0)
	v_fmac_f32_e32 v24, v104, v58
	v_pk_fma_f32 v[10:11], v[106:107], v[30:31], v[10:11] op_sel_hi:[0,1,1]
	v_pk_fma_f32 v[12:13], v[106:107], v[38:39], v[12:13] op_sel_hi:[0,1,1]
	v_pk_fma_f32 v[14:15], v[106:107], v[46:47], v[14:15] op_sel_hi:[0,1,1]
	v_pk_fma_f32 v[16:17], v[106:107], v[54:55], v[16:17] op_sel_hi:[0,1,1]
	v_fmac_f32_e32 v24, v106, v59
	v_pk_fma_f32 v[10:11], v[108:109], v[26:27], v[10:11] op_sel_hi:[0,1,1]
	v_pk_fma_f32 v[12:13], v[108:109], v[34:35], v[12:13] op_sel_hi:[0,1,1]
	v_pk_fma_f32 v[14:15], v[108:109], v[42:43], v[14:15] op_sel_hi:[0,1,1]
	v_pk_fma_f32 v[16:17], v[108:109], v[50:51], v[16:17] op_sel_hi:[0,1,1]
	v_fmac_f32_e32 v24, v108, v60
	v_pk_fma_f32 v[10:11], v[110:111], v[32:33], v[10:11] op_sel_hi:[0,1,1]
	v_pk_fma_f32 v[12:13], v[110:111], v[40:41], v[12:13] op_sel_hi:[0,1,1]
	v_pk_fma_f32 v[14:15], v[110:111], v[48:49], v[14:15] op_sel_hi:[0,1,1]
	v_pk_fma_f32 v[16:17], v[110:111], v[56:57], v[16:17] op_sel_hi:[0,1,1]
	v_fmac_f32_e32 v24, v110, v61
	v_add_u32_e32 v25, s11, v19
	v_add_u32_e32 v26, 0x11000, v25
	v_add_u32_e32 v30, 0x12000, v25
	v_add_u32_e32 v34, 0x13000, v25
	v_add_u32_e32 v38, 0x14000, v25
	v_add_u32_e32 v42, 0x15000, v25
	v_add_u32_e32 v46, 0x16000, v25
	v_add_u32_e32 v50, 0x17000, v25
	v_add_u32_e32 v54, 0x18000, v25
	v_add_u32_e32 v25, 0x19000, v25
	ds_read_b128 v[26:29], v26 offset:80
	ds_read_b128 v[30:33], v30 offset:80
	ds_read_b128 v[34:37], v34 offset:80
	ds_read_b128 v[38:41], v38 offset:80
	ds_read_b128 v[42:45], v42 offset:80
	ds_read_b128 v[46:49], v46 offset:80
	ds_read_b128 v[50:53], v50 offset:80
	ds_read_b128 v[54:57], v54 offset:80
	ds_read_b128 v[58:61], v25 offset:80
	s_waitcnt lgkmcnt(8)
	v_mov_b32_e32 v70, v26
	s_waitcnt lgkmcnt(7)
	v_mov_b32_e32 v71, v30
	v_mov_b32_e32 v30, v27
	v_mov_b32_e32 v26, v28
	v_mov_b32_e32 v27, v32
	v_mov_b32_e32 v32, v29
	s_waitcnt lgkmcnt(6)
	v_mov_b32_e32 v28, v34
	s_waitcnt lgkmcnt(5)
	v_mov_b32_e32 v29, v38
	v_mov_b32_e32 v38, v35
	v_mov_b32_e32 v34, v36
	v_mov_b32_e32 v35, v40
	v_mov_b32_e32 v40, v37
	s_waitcnt lgkmcnt(4)
	v_mov_b32_e32 v36, v42
	s_waitcnt lgkmcnt(3)
	v_mov_b32_e32 v37, v46
	v_mov_b32_e32 v46, v43
	v_mov_b32_e32 v42, v44
	v_mov_b32_e32 v43, v48
	v_mov_b32_e32 v48, v45
	s_waitcnt lgkmcnt(2)
	v_mov_b32_e32 v44, v50
	s_waitcnt lgkmcnt(1)
	v_mov_b32_e32 v45, v54
	v_mov_b32_e32 v54, v51
	v_mov_b32_e32 v50, v52
	v_mov_b32_e32 v51, v56
	v_mov_b32_e32 v56, v53
	s_waitcnt vmcnt(40)
	v_pk_fma_f32 v[10:11], v[112:113], v[70:71], v[10:11] op_sel_hi:[0,1,1]
	v_pk_fma_f32 v[12:13], v[112:113], v[28:29], v[12:13] op_sel_hi:[0,1,1]
	v_pk_fma_f32 v[14:15], v[112:113], v[36:37], v[14:15] op_sel_hi:[0,1,1]
	v_pk_fma_f32 v[16:17], v[112:113], v[44:45], v[16:17] op_sel_hi:[0,1,1]
	s_waitcnt lgkmcnt(0)
	v_fmac_f32_e32 v24, v112, v58
	v_pk_fma_f32 v[10:11], v[114:115], v[30:31], v[10:11] op_sel_hi:[0,1,1]
	v_pk_fma_f32 v[12:13], v[114:115], v[38:39], v[12:13] op_sel_hi:[0,1,1]
	v_pk_fma_f32 v[14:15], v[114:115], v[46:47], v[14:15] op_sel_hi:[0,1,1]
	v_pk_fma_f32 v[16:17], v[114:115], v[54:55], v[16:17] op_sel_hi:[0,1,1]
	v_fmac_f32_e32 v24, v114, v59
	v_pk_fma_f32 v[10:11], v[116:117], v[26:27], v[10:11] op_sel_hi:[0,1,1]
	v_pk_fma_f32 v[12:13], v[116:117], v[34:35], v[12:13] op_sel_hi:[0,1,1]
	v_pk_fma_f32 v[14:15], v[116:117], v[42:43], v[14:15] op_sel_hi:[0,1,1]
	v_pk_fma_f32 v[16:17], v[116:117], v[50:51], v[16:17] op_sel_hi:[0,1,1]
	v_fmac_f32_e32 v24, v116, v60
	v_pk_fma_f32 v[10:11], v[118:119], v[32:33], v[10:11] op_sel_hi:[0,1,1]
	v_pk_fma_f32 v[12:13], v[118:119], v[40:41], v[12:13] op_sel_hi:[0,1,1]
	v_pk_fma_f32 v[14:15], v[118:119], v[48:49], v[14:15] op_sel_hi:[0,1,1]
	v_pk_fma_f32 v[16:17], v[118:119], v[56:57], v[16:17] op_sel_hi:[0,1,1]
	v_fmac_f32_e32 v24, v118, v61
	v_add_u32_e32 v25, s11, v19
	v_add_u32_e32 v26, 0x11000, v25
	v_add_u32_e32 v30, 0x12000, v25
	v_add_u32_e32 v34, 0x13000, v25
	v_add_u32_e32 v38, 0x14000, v25
	v_add_u32_e32 v42, 0x15000, v25
	v_add_u32_e32 v46, 0x16000, v25
	v_add_u32_e32 v50, 0x17000, v25
	v_add_u32_e32 v54, 0x18000, v25
	v_add_u32_e32 v25, 0x19000, v25
	ds_read_b128 v[26:29], v26 offset:96
	ds_read_b128 v[30:33], v30 offset:96
	ds_read_b128 v[34:37], v34 offset:96
	ds_read_b128 v[38:41], v38 offset:96
	ds_read_b128 v[42:45], v42 offset:96
	ds_read_b128 v[46:49], v46 offset:96
	ds_read_b128 v[50:53], v50 offset:96
	ds_read_b128 v[54:57], v54 offset:96
	ds_read_b128 v[58:61], v25 offset:96
	s_waitcnt lgkmcnt(8)
	v_mov_b32_e32 v70, v26
	s_waitcnt lgkmcnt(7)
	v_mov_b32_e32 v71, v30
	v_mov_b32_e32 v30, v27
	v_mov_b32_e32 v26, v28
	v_mov_b32_e32 v27, v32
	v_mov_b32_e32 v32, v29
	s_waitcnt lgkmcnt(6)
	v_mov_b32_e32 v28, v34
	s_waitcnt lgkmcnt(5)
	v_mov_b32_e32 v29, v38
	v_mov_b32_e32 v38, v35
	v_mov_b32_e32 v34, v36
	v_mov_b32_e32 v35, v40
	v_mov_b32_e32 v40, v37
	s_waitcnt lgkmcnt(4)
	v_mov_b32_e32 v36, v42
	s_waitcnt lgkmcnt(3)
	v_mov_b32_e32 v37, v46
	v_mov_b32_e32 v46, v43
	v_mov_b32_e32 v42, v44
	v_mov_b32_e32 v43, v48
	v_mov_b32_e32 v48, v45
	s_waitcnt lgkmcnt(2)
	v_mov_b32_e32 v44, v50
	s_waitcnt lgkmcnt(1)
	v_mov_b32_e32 v45, v54
	v_mov_b32_e32 v54, v51
	v_mov_b32_e32 v50, v52
	v_mov_b32_e32 v51, v56
	v_mov_b32_e32 v56, v53
	s_waitcnt vmcnt(36)
	v_pk_fma_f32 v[10:11], v[120:121], v[70:71], v[10:11] op_sel_hi:[0,1,1]
	v_pk_fma_f32 v[12:13], v[120:121], v[28:29], v[12:13] op_sel_hi:[0,1,1]
	v_pk_fma_f32 v[14:15], v[120:121], v[36:37], v[14:15] op_sel_hi:[0,1,1]
	v_pk_fma_f32 v[16:17], v[120:121], v[44:45], v[16:17] op_sel_hi:[0,1,1]
	s_waitcnt lgkmcnt(0)
	v_fmac_f32_e32 v24, v120, v58
	v_pk_fma_f32 v[10:11], v[122:123], v[30:31], v[10:11] op_sel_hi:[0,1,1]
	v_pk_fma_f32 v[12:13], v[122:123], v[38:39], v[12:13] op_sel_hi:[0,1,1]
	v_pk_fma_f32 v[14:15], v[122:123], v[46:47], v[14:15] op_sel_hi:[0,1,1]
	v_pk_fma_f32 v[16:17], v[122:123], v[54:55], v[16:17] op_sel_hi:[0,1,1]
	v_fmac_f32_e32 v24, v122, v59
	v_pk_fma_f32 v[10:11], v[124:125], v[26:27], v[10:11] op_sel_hi:[0,1,1]
	v_pk_fma_f32 v[12:13], v[124:125], v[34:35], v[12:13] op_sel_hi:[0,1,1]
	v_pk_fma_f32 v[14:15], v[124:125], v[42:43], v[14:15] op_sel_hi:[0,1,1]
	v_pk_fma_f32 v[16:17], v[124:125], v[50:51], v[16:17] op_sel_hi:[0,1,1]
	v_fmac_f32_e32 v24, v124, v60
	v_pk_fma_f32 v[10:11], v[126:127], v[32:33], v[10:11] op_sel_hi:[0,1,1]
	v_pk_fma_f32 v[12:13], v[126:127], v[40:41], v[12:13] op_sel_hi:[0,1,1]
	v_pk_fma_f32 v[14:15], v[126:127], v[48:49], v[14:15] op_sel_hi:[0,1,1]
	v_pk_fma_f32 v[16:17], v[126:127], v[56:57], v[16:17] op_sel_hi:[0,1,1]
	v_fmac_f32_e32 v24, v126, v61
	v_add_u32_e32 v25, s11, v19
	v_add_u32_e32 v26, 0x11000, v25
	v_add_u32_e32 v30, 0x12000, v25
	v_add_u32_e32 v34, 0x13000, v25
	v_add_u32_e32 v38, 0x14000, v25
	v_add_u32_e32 v42, 0x15000, v25
	v_add_u32_e32 v46, 0x16000, v25
	v_add_u32_e32 v50, 0x17000, v25
	v_add_u32_e32 v54, 0x18000, v25
	v_add_u32_e32 v25, 0x19000, v25
	ds_read_b128 v[26:29], v26 offset:112
	ds_read_b128 v[30:33], v30 offset:112
	ds_read_b128 v[34:37], v34 offset:112
	ds_read_b128 v[38:41], v38 offset:112
	ds_read_b128 v[42:45], v42 offset:112
	ds_read_b128 v[46:49], v46 offset:112
	ds_read_b128 v[50:53], v50 offset:112
	ds_read_b128 v[54:57], v54 offset:112
	ds_read_b128 v[58:61], v25 offset:112
	s_waitcnt lgkmcnt(8)
	v_mov_b32_e32 v70, v26
	s_waitcnt lgkmcnt(7)
	v_mov_b32_e32 v71, v30
	v_mov_b32_e32 v30, v27
	v_mov_b32_e32 v26, v28
	v_mov_b32_e32 v27, v32
	v_mov_b32_e32 v32, v29
	s_waitcnt lgkmcnt(6)
	v_mov_b32_e32 v28, v34
	s_waitcnt lgkmcnt(5)
	v_mov_b32_e32 v29, v38
	v_mov_b32_e32 v38, v35
	v_mov_b32_e32 v34, v36
	v_mov_b32_e32 v35, v40
	v_mov_b32_e32 v40, v37
	s_waitcnt lgkmcnt(4)
	v_mov_b32_e32 v36, v42
	s_waitcnt lgkmcnt(3)
	v_mov_b32_e32 v37, v46
	v_mov_b32_e32 v46, v43
	v_mov_b32_e32 v42, v44
	v_mov_b32_e32 v43, v48
	v_mov_b32_e32 v48, v45
	s_waitcnt lgkmcnt(2)
	v_mov_b32_e32 v44, v50
	s_waitcnt lgkmcnt(1)
	v_mov_b32_e32 v45, v54
	v_mov_b32_e32 v54, v51
	v_mov_b32_e32 v50, v52
	v_mov_b32_e32 v51, v56
	v_mov_b32_e32 v56, v53
	s_waitcnt vmcnt(32)
	v_pk_fma_f32 v[10:11], v[128:129], v[70:71], v[10:11] op_sel_hi:[0,1,1]
	v_pk_fma_f32 v[12:13], v[128:129], v[28:29], v[12:13] op_sel_hi:[0,1,1]
	v_pk_fma_f32 v[14:15], v[128:129], v[36:37], v[14:15] op_sel_hi:[0,1,1]
	v_pk_fma_f32 v[16:17], v[128:129], v[44:45], v[16:17] op_sel_hi:[0,1,1]
	s_waitcnt lgkmcnt(0)
	v_fmac_f32_e32 v24, v128, v58
	v_pk_fma_f32 v[10:11], v[130:131], v[30:31], v[10:11] op_sel_hi:[0,1,1]
	v_pk_fma_f32 v[12:13], v[130:131], v[38:39], v[12:13] op_sel_hi:[0,1,1]
	v_pk_fma_f32 v[14:15], v[130:131], v[46:47], v[14:15] op_sel_hi:[0,1,1]
	v_pk_fma_f32 v[16:17], v[130:131], v[54:55], v[16:17] op_sel_hi:[0,1,1]
	v_fmac_f32_e32 v24, v130, v59
	v_pk_fma_f32 v[10:11], v[132:133], v[26:27], v[10:11] op_sel_hi:[0,1,1]
	v_pk_fma_f32 v[12:13], v[132:133], v[34:35], v[12:13] op_sel_hi:[0,1,1]
	v_pk_fma_f32 v[14:15], v[132:133], v[42:43], v[14:15] op_sel_hi:[0,1,1]
	v_pk_fma_f32 v[16:17], v[132:133], v[50:51], v[16:17] op_sel_hi:[0,1,1]
	v_fmac_f32_e32 v24, v132, v60
	v_pk_fma_f32 v[10:11], v[134:135], v[32:33], v[10:11] op_sel_hi:[0,1,1]
	v_pk_fma_f32 v[12:13], v[134:135], v[40:41], v[12:13] op_sel_hi:[0,1,1]
	v_pk_fma_f32 v[14:15], v[134:135], v[48:49], v[14:15] op_sel_hi:[0,1,1]
	v_pk_fma_f32 v[16:17], v[134:135], v[56:57], v[16:17] op_sel_hi:[0,1,1]
	v_fmac_f32_e32 v24, v134, v61
	s_cmpk_eq_i32 s11, 0x300
	s_cselect_b32 s100, 0xffe80000, 0
	s_cselect_b32 s101, -1, 0
	v_lshl_add_u64 v[8:9], v[8:9], 0, s[100:101]
	global_load_dword v72, v[8:9], off
	v_lshl_add_u64 v[8:9], v[8:9], 0, s[8:9]
	global_load_dword v74, v[8:9], off
	v_lshl_add_u64 v[8:9], v[8:9], 0, s[8:9]
	global_load_dword v76, v[8:9], off
	v_lshl_add_u64 v[8:9], v[8:9], 0, s[8:9]
	global_load_dword v78, v[8:9], off
	v_lshl_add_u64 v[8:9], v[8:9], 0, s[8:9]
	global_load_dword v80, v[8:9], off
	v_lshl_add_u64 v[8:9], v[8:9], 0, s[8:9]
	global_load_dword v82, v[8:9], off
	v_lshl_add_u64 v[8:9], v[8:9], 0, s[8:9]
	global_load_dword v84, v[8:9], off
	v_lshl_add_u64 v[8:9], v[8:9], 0, s[8:9]
	global_load_dword v86, v[8:9], off
	v_lshl_add_u64 v[8:9], v[8:9], 0, s[8:9]
	global_load_dword v88, v[8:9], off
	v_lshl_add_u64 v[8:9], v[8:9], 0, s[8:9]
	global_load_dword v90, v[8:9], off
	v_lshl_add_u64 v[8:9], v[8:9], 0, s[8:9]
	global_load_dword v92, v[8:9], off
	v_lshl_add_u64 v[8:9], v[8:9], 0, s[8:9]
	global_load_dword v94, v[8:9], off
	v_lshl_add_u64 v[8:9], v[8:9], 0, s[8:9]
	global_load_dword v96, v[8:9], off
	v_lshl_add_u64 v[8:9], v[8:9], 0, s[8:9]
	global_load_dword v98, v[8:9], off
	v_lshl_add_u64 v[8:9], v[8:9], 0, s[8:9]
	global_load_dword v100, v[8:9], off
	v_lshl_add_u64 v[8:9], v[8:9], 0, s[8:9]
	global_load_dword v102, v[8:9], off
	v_lshl_add_u64 v[8:9], v[8:9], 0, s[8:9]
	global_load_dword v104, v[8:9], off
	v_lshl_add_u64 v[8:9], v[8:9], 0, s[8:9]
	global_load_dword v106, v[8:9], off
	v_lshl_add_u64 v[8:9], v[8:9], 0, s[8:9]
	global_load_dword v108, v[8:9], off
	v_lshl_add_u64 v[8:9], v[8:9], 0, s[8:9]
	global_load_dword v110, v[8:9], off
	v_lshl_add_u64 v[8:9], v[8:9], 0, s[8:9]
	global_load_dword v112, v[8:9], off
	v_lshl_add_u64 v[8:9], v[8:9], 0, s[8:9]
	global_load_dword v114, v[8:9], off
	v_lshl_add_u64 v[8:9], v[8:9], 0, s[8:9]
	global_load_dword v116, v[8:9], off
	v_lshl_add_u64 v[8:9], v[8:9], 0, s[8:9]
	global_load_dword v118, v[8:9], off
	v_lshl_add_u64 v[8:9], v[8:9], 0, s[8:9]
	global_load_dword v120, v[8:9], off
	v_lshl_add_u64 v[8:9], v[8:9], 0, s[8:9]
	global_load_dword v122, v[8:9], off
	v_lshl_add_u64 v[8:9], v[8:9], 0, s[8:9]
	global_load_dword v124, v[8:9], off
	v_lshl_add_u64 v[8:9], v[8:9], 0, s[8:9]
	global_load_dword v126, v[8:9], off
	v_lshl_add_u64 v[8:9], v[8:9], 0, s[8:9]
	global_load_dword v128, v[8:9], off
	v_lshl_add_u64 v[8:9], v[8:9], 0, s[8:9]
	global_load_dword v130, v[8:9], off
	v_lshl_add_u64 v[8:9], v[8:9], 0, s[8:9]
	global_load_dword v132, v[8:9], off
	v_lshl_add_u64 v[8:9], v[8:9], 0, s[8:9]
	global_load_dword v134, v[8:9], off
	v_lshl_add_u64 v[8:9], v[8:9], 0, s[8:9]
	v_add_u32_e32 v25, s11, v19
	v_add_u32_e32 v26, 0x11000, v25
	v_add_u32_e32 v30, 0x12000, v25
	v_add_u32_e32 v34, 0x13000, v25
	v_add_u32_e32 v38, 0x14000, v25
	v_add_u32_e32 v42, 0x15000, v25
	v_add_u32_e32 v46, 0x16000, v25
	v_add_u32_e32 v50, 0x17000, v25
	v_add_u32_e32 v54, 0x18000, v25
	v_add_u32_e32 v25, 0x19000, v25
	ds_read_b128 v[26:29], v26 offset:128
	ds_read_b128 v[30:33], v30 offset:128
	ds_read_b128 v[34:37], v34 offset:128
	ds_read_b128 v[38:41], v38 offset:128
	ds_read_b128 v[42:45], v42 offset:128
	ds_read_b128 v[46:49], v46 offset:128
	ds_read_b128 v[50:53], v50 offset:128
	ds_read_b128 v[54:57], v54 offset:128
	ds_read_b128 v[58:61], v25 offset:128
	s_waitcnt lgkmcnt(8)
	v_mov_b32_e32 v70, v26
	s_waitcnt lgkmcnt(7)
	v_mov_b32_e32 v71, v30
	v_mov_b32_e32 v30, v27
	v_mov_b32_e32 v26, v28
	v_mov_b32_e32 v27, v32
	v_mov_b32_e32 v32, v29
	s_waitcnt lgkmcnt(6)
	v_mov_b32_e32 v28, v34
	s_waitcnt lgkmcnt(5)
	v_mov_b32_e32 v29, v38
	v_mov_b32_e32 v38, v35
	v_mov_b32_e32 v34, v36
	v_mov_b32_e32 v35, v40
	v_mov_b32_e32 v40, v37
	s_waitcnt lgkmcnt(4)
	v_mov_b32_e32 v36, v42
	s_waitcnt lgkmcnt(3)
	v_mov_b32_e32 v37, v46
	v_mov_b32_e32 v46, v43
	v_mov_b32_e32 v42, v44
	v_mov_b32_e32 v43, v48
	v_mov_b32_e32 v48, v45
	s_waitcnt lgkmcnt(2)
	v_mov_b32_e32 v44, v50
	s_waitcnt lgkmcnt(1)
	v_mov_b32_e32 v45, v54
	v_mov_b32_e32 v54, v51
	v_mov_b32_e32 v50, v52
	v_mov_b32_e32 v51, v56
	v_mov_b32_e32 v56, v53
	s_waitcnt vmcnt(60)
	v_pk_fma_f32 v[10:11], v[136:137], v[70:71], v[10:11] op_sel_hi:[0,1,1]
	v_pk_fma_f32 v[12:13], v[136:137], v[28:29], v[12:13] op_sel_hi:[0,1,1]
	v_pk_fma_f32 v[14:15], v[136:137], v[36:37], v[14:15] op_sel_hi:[0,1,1]
	v_pk_fma_f32 v[16:17], v[136:137], v[44:45], v[16:17] op_sel_hi:[0,1,1]
	s_waitcnt lgkmcnt(0)
	v_fmac_f32_e32 v24, v136, v58
	v_pk_fma_f32 v[10:11], v[138:139], v[30:31], v[10:11] op_sel_hi:[0,1,1]
	v_pk_fma_f32 v[12:13], v[138:139], v[38:39], v[12:13] op_sel_hi:[0,1,1]
	v_pk_fma_f32 v[14:15], v[138:139], v[46:47], v[14:15] op_sel_hi:[0,1,1]
	v_pk_fma_f32 v[16:17], v[138:139], v[54:55], v[16:17] op_sel_hi:[0,1,1]
	v_fmac_f32_e32 v24, v138, v59
	v_pk_fma_f32 v[10:11], v[140:141], v[26:27], v[10:11] op_sel_hi:[0,1,1]
	v_pk_fma_f32 v[12:13], v[140:141], v[34:35], v[12:13] op_sel_hi:[0,1,1]
	v_pk_fma_f32 v[14:15], v[140:141], v[42:43], v[14:15] op_sel_hi:[0,1,1]
	v_pk_fma_f32 v[16:17], v[140:141], v[50:51], v[16:17] op_sel_hi:[0,1,1]
	v_fmac_f32_e32 v24, v140, v60
	v_pk_fma_f32 v[10:11], v[142:143], v[32:33], v[10:11] op_sel_hi:[0,1,1]
	v_pk_fma_f32 v[12:13], v[142:143], v[40:41], v[12:13] op_sel_hi:[0,1,1]
	v_pk_fma_f32 v[14:15], v[142:143], v[48:49], v[14:15] op_sel_hi:[0,1,1]
	v_pk_fma_f32 v[16:17], v[142:143], v[56:57], v[16:17] op_sel_hi:[0,1,1]
	v_fmac_f32_e32 v24, v142, v61
	v_add_u32_e32 v25, s11, v19
	v_add_u32_e32 v26, 0x11000, v25
	v_add_u32_e32 v30, 0x12000, v25
	v_add_u32_e32 v34, 0x13000, v25
	v_add_u32_e32 v38, 0x14000, v25
	v_add_u32_e32 v42, 0x15000, v25
	v_add_u32_e32 v46, 0x16000, v25
	v_add_u32_e32 v50, 0x17000, v25
	v_add_u32_e32 v54, 0x18000, v25
	v_add_u32_e32 v25, 0x19000, v25
	ds_read_b128 v[26:29], v26 offset:144
	ds_read_b128 v[30:33], v30 offset:144
	ds_read_b128 v[34:37], v34 offset:144
	ds_read_b128 v[38:41], v38 offset:144
	ds_read_b128 v[42:45], v42 offset:144
	ds_read_b128 v[46:49], v46 offset:144
	ds_read_b128 v[50:53], v50 offset:144
	ds_read_b128 v[54:57], v54 offset:144
	ds_read_b128 v[58:61], v25 offset:144
	s_waitcnt lgkmcnt(8)
	v_mov_b32_e32 v70, v26
	s_waitcnt lgkmcnt(7)
	v_mov_b32_e32 v71, v30
	v_mov_b32_e32 v30, v27
	v_mov_b32_e32 v26, v28
	v_mov_b32_e32 v27, v32
	v_mov_b32_e32 v32, v29
	s_waitcnt lgkmcnt(6)
	v_mov_b32_e32 v28, v34
	s_waitcnt lgkmcnt(5)
	v_mov_b32_e32 v29, v38
	v_mov_b32_e32 v38, v35
	v_mov_b32_e32 v34, v36
	v_mov_b32_e32 v35, v40
	v_mov_b32_e32 v40, v37
	s_waitcnt lgkmcnt(4)
	v_mov_b32_e32 v36, v42
	s_waitcnt lgkmcnt(3)
	v_mov_b32_e32 v37, v46
	v_mov_b32_e32 v46, v43
	v_mov_b32_e32 v42, v44
	v_mov_b32_e32 v43, v48
	v_mov_b32_e32 v48, v45
	s_waitcnt lgkmcnt(2)
	v_mov_b32_e32 v44, v50
	s_waitcnt lgkmcnt(1)
	v_mov_b32_e32 v45, v54
	v_mov_b32_e32 v54, v51
	v_mov_b32_e32 v50, v52
	v_mov_b32_e32 v51, v56
	v_mov_b32_e32 v56, v53
	s_waitcnt vmcnt(56)
	v_pk_fma_f32 v[10:11], v[144:145], v[70:71], v[10:11] op_sel_hi:[0,1,1]
	v_pk_fma_f32 v[12:13], v[144:145], v[28:29], v[12:13] op_sel_hi:[0,1,1]
	v_pk_fma_f32 v[14:15], v[144:145], v[36:37], v[14:15] op_sel_hi:[0,1,1]
	v_pk_fma_f32 v[16:17], v[144:145], v[44:45], v[16:17] op_sel_hi:[0,1,1]
	s_waitcnt lgkmcnt(0)
	v_fmac_f32_e32 v24, v144, v58
	v_pk_fma_f32 v[10:11], v[146:147], v[30:31], v[10:11] op_sel_hi:[0,1,1]
	v_pk_fma_f32 v[12:13], v[146:147], v[38:39], v[12:13] op_sel_hi:[0,1,1]
	v_pk_fma_f32 v[14:15], v[146:147], v[46:47], v[14:15] op_sel_hi:[0,1,1]
	v_pk_fma_f32 v[16:17], v[146:147], v[54:55], v[16:17] op_sel_hi:[0,1,1]
	v_fmac_f32_e32 v24, v146, v59
	v_pk_fma_f32 v[10:11], v[148:149], v[26:27], v[10:11] op_sel_hi:[0,1,1]
	v_pk_fma_f32 v[12:13], v[148:149], v[34:35], v[12:13] op_sel_hi:[0,1,1]
	v_pk_fma_f32 v[14:15], v[148:149], v[42:43], v[14:15] op_sel_hi:[0,1,1]
	v_pk_fma_f32 v[16:17], v[148:149], v[50:51], v[16:17] op_sel_hi:[0,1,1]
	v_fmac_f32_e32 v24, v148, v60
	v_pk_fma_f32 v[10:11], v[150:151], v[32:33], v[10:11] op_sel_hi:[0,1,1]
	v_pk_fma_f32 v[12:13], v[150:151], v[40:41], v[12:13] op_sel_hi:[0,1,1]
	v_pk_fma_f32 v[14:15], v[150:151], v[48:49], v[14:15] op_sel_hi:[0,1,1]
	v_pk_fma_f32 v[16:17], v[150:151], v[56:57], v[16:17] op_sel_hi:[0,1,1]
	v_fmac_f32_e32 v24, v150, v61
	v_add_u32_e32 v25, s11, v19
	v_add_u32_e32 v26, 0x11000, v25
	v_add_u32_e32 v30, 0x12000, v25
	v_add_u32_e32 v34, 0x13000, v25
	v_add_u32_e32 v38, 0x14000, v25
	v_add_u32_e32 v42, 0x15000, v25
	v_add_u32_e32 v46, 0x16000, v25
	v_add_u32_e32 v50, 0x17000, v25
	v_add_u32_e32 v54, 0x18000, v25
	v_add_u32_e32 v25, 0x19000, v25
	ds_read_b128 v[26:29], v26 offset:160
	ds_read_b128 v[30:33], v30 offset:160
	ds_read_b128 v[34:37], v34 offset:160
	ds_read_b128 v[38:41], v38 offset:160
	ds_read_b128 v[42:45], v42 offset:160
	ds_read_b128 v[46:49], v46 offset:160
	ds_read_b128 v[50:53], v50 offset:160
	ds_read_b128 v[54:57], v54 offset:160
	ds_read_b128 v[58:61], v25 offset:160
	s_waitcnt lgkmcnt(8)
	v_mov_b32_e32 v70, v26
	s_waitcnt lgkmcnt(7)
	v_mov_b32_e32 v71, v30
	v_mov_b32_e32 v30, v27
	v_mov_b32_e32 v26, v28
	v_mov_b32_e32 v27, v32
	v_mov_b32_e32 v32, v29
	s_waitcnt lgkmcnt(6)
	v_mov_b32_e32 v28, v34
	s_waitcnt lgkmcnt(5)
	v_mov_b32_e32 v29, v38
	v_mov_b32_e32 v38, v35
	v_mov_b32_e32 v34, v36
	v_mov_b32_e32 v35, v40
	v_mov_b32_e32 v40, v37
	s_waitcnt lgkmcnt(4)
	v_mov_b32_e32 v36, v42
	s_waitcnt lgkmcnt(3)
	v_mov_b32_e32 v37, v46
	v_mov_b32_e32 v46, v43
	v_mov_b32_e32 v42, v44
	v_mov_b32_e32 v43, v48
	v_mov_b32_e32 v48, v45
	s_waitcnt lgkmcnt(2)
	v_mov_b32_e32 v44, v50
	s_waitcnt lgkmcnt(1)
	v_mov_b32_e32 v45, v54
	v_mov_b32_e32 v54, v51
	v_mov_b32_e32 v50, v52
	v_mov_b32_e32 v51, v56
	v_mov_b32_e32 v56, v53
	s_waitcnt vmcnt(52)
	v_pk_fma_f32 v[10:11], v[152:153], v[70:71], v[10:11] op_sel_hi:[0,1,1]
	v_pk_fma_f32 v[12:13], v[152:153], v[28:29], v[12:13] op_sel_hi:[0,1,1]
	v_pk_fma_f32 v[14:15], v[152:153], v[36:37], v[14:15] op_sel_hi:[0,1,1]
	v_pk_fma_f32 v[16:17], v[152:153], v[44:45], v[16:17] op_sel_hi:[0,1,1]
	s_waitcnt lgkmcnt(0)
	v_fmac_f32_e32 v24, v152, v58
	v_pk_fma_f32 v[10:11], v[154:155], v[30:31], v[10:11] op_sel_hi:[0,1,1]
	v_pk_fma_f32 v[12:13], v[154:155], v[38:39], v[12:13] op_sel_hi:[0,1,1]
	v_pk_fma_f32 v[14:15], v[154:155], v[46:47], v[14:15] op_sel_hi:[0,1,1]
	v_pk_fma_f32 v[16:17], v[154:155], v[54:55], v[16:17] op_sel_hi:[0,1,1]
	v_fmac_f32_e32 v24, v154, v59
	v_pk_fma_f32 v[10:11], v[156:157], v[26:27], v[10:11] op_sel_hi:[0,1,1]
	v_pk_fma_f32 v[12:13], v[156:157], v[34:35], v[12:13] op_sel_hi:[0,1,1]
	v_pk_fma_f32 v[14:15], v[156:157], v[42:43], v[14:15] op_sel_hi:[0,1,1]
	v_pk_fma_f32 v[16:17], v[156:157], v[50:51], v[16:17] op_sel_hi:[0,1,1]
	v_fmac_f32_e32 v24, v156, v60
	v_pk_fma_f32 v[10:11], v[158:159], v[32:33], v[10:11] op_sel_hi:[0,1,1]
	v_pk_fma_f32 v[12:13], v[158:159], v[40:41], v[12:13] op_sel_hi:[0,1,1]
	v_pk_fma_f32 v[14:15], v[158:159], v[48:49], v[14:15] op_sel_hi:[0,1,1]
	v_pk_fma_f32 v[16:17], v[158:159], v[56:57], v[16:17] op_sel_hi:[0,1,1]
	v_fmac_f32_e32 v24, v158, v61
	v_add_u32_e32 v25, s11, v19
	v_add_u32_e32 v26, 0x11000, v25
	v_add_u32_e32 v30, 0x12000, v25
	v_add_u32_e32 v34, 0x13000, v25
	v_add_u32_e32 v38, 0x14000, v25
	v_add_u32_e32 v42, 0x15000, v25
	v_add_u32_e32 v46, 0x16000, v25
	v_add_u32_e32 v50, 0x17000, v25
	v_add_u32_e32 v54, 0x18000, v25
	v_add_u32_e32 v25, 0x19000, v25
	ds_read_b128 v[26:29], v26 offset:176
	ds_read_b128 v[30:33], v30 offset:176
	ds_read_b128 v[34:37], v34 offset:176
	ds_read_b128 v[38:41], v38 offset:176
	ds_read_b128 v[42:45], v42 offset:176
	ds_read_b128 v[46:49], v46 offset:176
	ds_read_b128 v[50:53], v50 offset:176
	ds_read_b128 v[54:57], v54 offset:176
	ds_read_b128 v[58:61], v25 offset:176
	s_waitcnt lgkmcnt(8)
	v_mov_b32_e32 v70, v26
	s_waitcnt lgkmcnt(7)
	v_mov_b32_e32 v71, v30
	v_mov_b32_e32 v30, v27
	v_mov_b32_e32 v26, v28
	v_mov_b32_e32 v27, v32
	v_mov_b32_e32 v32, v29
	s_waitcnt lgkmcnt(6)
	v_mov_b32_e32 v28, v34
	s_waitcnt lgkmcnt(5)
	v_mov_b32_e32 v29, v38
	v_mov_b32_e32 v38, v35
	v_mov_b32_e32 v34, v36
	v_mov_b32_e32 v35, v40
	v_mov_b32_e32 v40, v37
	s_waitcnt lgkmcnt(4)
	v_mov_b32_e32 v36, v42
	s_waitcnt lgkmcnt(3)
	v_mov_b32_e32 v37, v46
	v_mov_b32_e32 v46, v43
	v_mov_b32_e32 v42, v44
	v_mov_b32_e32 v43, v48
	v_mov_b32_e32 v48, v45
	s_waitcnt lgkmcnt(2)
	v_mov_b32_e32 v44, v50
	s_waitcnt lgkmcnt(1)
	v_mov_b32_e32 v45, v54
	v_mov_b32_e32 v54, v51
	v_mov_b32_e32 v50, v52
	v_mov_b32_e32 v51, v56
	v_mov_b32_e32 v56, v53
	s_waitcnt vmcnt(48)
	v_pk_fma_f32 v[10:11], v[160:161], v[70:71], v[10:11] op_sel_hi:[0,1,1]
	v_pk_fma_f32 v[12:13], v[160:161], v[28:29], v[12:13] op_sel_hi:[0,1,1]
	v_pk_fma_f32 v[14:15], v[160:161], v[36:37], v[14:15] op_sel_hi:[0,1,1]
	v_pk_fma_f32 v[16:17], v[160:161], v[44:45], v[16:17] op_sel_hi:[0,1,1]
	s_waitcnt lgkmcnt(0)
	v_fmac_f32_e32 v24, v160, v58
	v_pk_fma_f32 v[10:11], v[162:163], v[30:31], v[10:11] op_sel_hi:[0,1,1]
	v_pk_fma_f32 v[12:13], v[162:163], v[38:39], v[12:13] op_sel_hi:[0,1,1]
	v_pk_fma_f32 v[14:15], v[162:163], v[46:47], v[14:15] op_sel_hi:[0,1,1]
	v_pk_fma_f32 v[16:17], v[162:163], v[54:55], v[16:17] op_sel_hi:[0,1,1]
	v_fmac_f32_e32 v24, v162, v59
	v_pk_fma_f32 v[10:11], v[164:165], v[26:27], v[10:11] op_sel_hi:[0,1,1]
	v_pk_fma_f32 v[12:13], v[164:165], v[34:35], v[12:13] op_sel_hi:[0,1,1]
	v_pk_fma_f32 v[14:15], v[164:165], v[42:43], v[14:15] op_sel_hi:[0,1,1]
	v_pk_fma_f32 v[16:17], v[164:165], v[50:51], v[16:17] op_sel_hi:[0,1,1]
	v_fmac_f32_e32 v24, v164, v60
	v_pk_fma_f32 v[10:11], v[166:167], v[32:33], v[10:11] op_sel_hi:[0,1,1]
	v_pk_fma_f32 v[12:13], v[166:167], v[40:41], v[12:13] op_sel_hi:[0,1,1]
	v_pk_fma_f32 v[14:15], v[166:167], v[48:49], v[14:15] op_sel_hi:[0,1,1]
	v_pk_fma_f32 v[16:17], v[166:167], v[56:57], v[16:17] op_sel_hi:[0,1,1]
	v_fmac_f32_e32 v24, v166, v61
	v_add_u32_e32 v25, s11, v19
	v_add_u32_e32 v26, 0x11000, v25
	v_add_u32_e32 v30, 0x12000, v25
	v_add_u32_e32 v34, 0x13000, v25
	v_add_u32_e32 v38, 0x14000, v25
	v_add_u32_e32 v42, 0x15000, v25
	v_add_u32_e32 v46, 0x16000, v25
	v_add_u32_e32 v50, 0x17000, v25
	v_add_u32_e32 v54, 0x18000, v25
	v_add_u32_e32 v25, 0x19000, v25
	ds_read_b128 v[26:29], v26 offset:192
	ds_read_b128 v[30:33], v30 offset:192
	ds_read_b128 v[34:37], v34 offset:192
	ds_read_b128 v[38:41], v38 offset:192
	ds_read_b128 v[42:45], v42 offset:192
	ds_read_b128 v[46:49], v46 offset:192
	ds_read_b128 v[50:53], v50 offset:192
	ds_read_b128 v[54:57], v54 offset:192
	ds_read_b128 v[58:61], v25 offset:192
	s_waitcnt lgkmcnt(8)
	v_mov_b32_e32 v70, v26
	s_waitcnt lgkmcnt(7)
	v_mov_b32_e32 v71, v30
	v_mov_b32_e32 v30, v27
	v_mov_b32_e32 v26, v28
	v_mov_b32_e32 v27, v32
	v_mov_b32_e32 v32, v29
	s_waitcnt lgkmcnt(6)
	v_mov_b32_e32 v28, v34
	s_waitcnt lgkmcnt(5)
	v_mov_b32_e32 v29, v38
	v_mov_b32_e32 v38, v35
	v_mov_b32_e32 v34, v36
	v_mov_b32_e32 v35, v40
	v_mov_b32_e32 v40, v37
	s_waitcnt lgkmcnt(4)
	v_mov_b32_e32 v36, v42
	s_waitcnt lgkmcnt(3)
	v_mov_b32_e32 v37, v46
	v_mov_b32_e32 v46, v43
	v_mov_b32_e32 v42, v44
	v_mov_b32_e32 v43, v48
	v_mov_b32_e32 v48, v45
	s_waitcnt lgkmcnt(2)
	v_mov_b32_e32 v44, v50
	s_waitcnt lgkmcnt(1)
	v_mov_b32_e32 v45, v54
	v_mov_b32_e32 v54, v51
	v_mov_b32_e32 v50, v52
	v_mov_b32_e32 v51, v56
	v_mov_b32_e32 v56, v53
	s_waitcnt vmcnt(44)
	v_pk_fma_f32 v[10:11], v[168:169], v[70:71], v[10:11] op_sel_hi:[0,1,1]
	v_pk_fma_f32 v[12:13], v[168:169], v[28:29], v[12:13] op_sel_hi:[0,1,1]
	v_pk_fma_f32 v[14:15], v[168:169], v[36:37], v[14:15] op_sel_hi:[0,1,1]
	v_pk_fma_f32 v[16:17], v[168:169], v[44:45], v[16:17] op_sel_hi:[0,1,1]
	s_waitcnt lgkmcnt(0)
	v_fmac_f32_e32 v24, v168, v58
	v_pk_fma_f32 v[10:11], v[170:171], v[30:31], v[10:11] op_sel_hi:[0,1,1]
	v_pk_fma_f32 v[12:13], v[170:171], v[38:39], v[12:13] op_sel_hi:[0,1,1]
	v_pk_fma_f32 v[14:15], v[170:171], v[46:47], v[14:15] op_sel_hi:[0,1,1]
	v_pk_fma_f32 v[16:17], v[170:171], v[54:55], v[16:17] op_sel_hi:[0,1,1]
	v_fmac_f32_e32 v24, v170, v59
	v_pk_fma_f32 v[10:11], v[172:173], v[26:27], v[10:11] op_sel_hi:[0,1,1]
	v_pk_fma_f32 v[12:13], v[172:173], v[34:35], v[12:13] op_sel_hi:[0,1,1]
	v_pk_fma_f32 v[14:15], v[172:173], v[42:43], v[14:15] op_sel_hi:[0,1,1]
	v_pk_fma_f32 v[16:17], v[172:173], v[50:51], v[16:17] op_sel_hi:[0,1,1]
	v_fmac_f32_e32 v24, v172, v60
	v_pk_fma_f32 v[10:11], v[174:175], v[32:33], v[10:11] op_sel_hi:[0,1,1]
	v_pk_fma_f32 v[12:13], v[174:175], v[40:41], v[12:13] op_sel_hi:[0,1,1]
	v_pk_fma_f32 v[14:15], v[174:175], v[48:49], v[14:15] op_sel_hi:[0,1,1]
	v_pk_fma_f32 v[16:17], v[174:175], v[56:57], v[16:17] op_sel_hi:[0,1,1]
	v_fmac_f32_e32 v24, v174, v61
	v_add_u32_e32 v25, s11, v19
	v_add_u32_e32 v26, 0x11000, v25
	v_add_u32_e32 v30, 0x12000, v25
	v_add_u32_e32 v34, 0x13000, v25
	v_add_u32_e32 v38, 0x14000, v25
	v_add_u32_e32 v42, 0x15000, v25
	v_add_u32_e32 v46, 0x16000, v25
	v_add_u32_e32 v50, 0x17000, v25
	v_add_u32_e32 v54, 0x18000, v25
	v_add_u32_e32 v25, 0x19000, v25
	ds_read_b128 v[26:29], v26 offset:208
	ds_read_b128 v[30:33], v30 offset:208
	ds_read_b128 v[34:37], v34 offset:208
	ds_read_b128 v[38:41], v38 offset:208
	ds_read_b128 v[42:45], v42 offset:208
	ds_read_b128 v[46:49], v46 offset:208
	ds_read_b128 v[50:53], v50 offset:208
	ds_read_b128 v[54:57], v54 offset:208
	ds_read_b128 v[58:61], v25 offset:208
	s_waitcnt lgkmcnt(8)
	v_mov_b32_e32 v70, v26
	s_waitcnt lgkmcnt(7)
	v_mov_b32_e32 v71, v30
	v_mov_b32_e32 v30, v27
	v_mov_b32_e32 v26, v28
	v_mov_b32_e32 v27, v32
	v_mov_b32_e32 v32, v29
	s_waitcnt lgkmcnt(6)
	v_mov_b32_e32 v28, v34
	s_waitcnt lgkmcnt(5)
	v_mov_b32_e32 v29, v38
	v_mov_b32_e32 v38, v35
	v_mov_b32_e32 v34, v36
	v_mov_b32_e32 v35, v40
	v_mov_b32_e32 v40, v37
	s_waitcnt lgkmcnt(4)
	v_mov_b32_e32 v36, v42
	s_waitcnt lgkmcnt(3)
	v_mov_b32_e32 v37, v46
	v_mov_b32_e32 v46, v43
	v_mov_b32_e32 v42, v44
	v_mov_b32_e32 v43, v48
	v_mov_b32_e32 v48, v45
	s_waitcnt lgkmcnt(2)
	v_mov_b32_e32 v44, v50
	s_waitcnt lgkmcnt(1)
	v_mov_b32_e32 v45, v54
	v_mov_b32_e32 v54, v51
	v_mov_b32_e32 v50, v52
	v_mov_b32_e32 v51, v56
	v_mov_b32_e32 v56, v53
	s_waitcnt vmcnt(40)
	v_pk_fma_f32 v[10:11], v[176:177], v[70:71], v[10:11] op_sel_hi:[0,1,1]
	v_pk_fma_f32 v[12:13], v[176:177], v[28:29], v[12:13] op_sel_hi:[0,1,1]
	v_pk_fma_f32 v[14:15], v[176:177], v[36:37], v[14:15] op_sel_hi:[0,1,1]
	v_pk_fma_f32 v[16:17], v[176:177], v[44:45], v[16:17] op_sel_hi:[0,1,1]
	s_waitcnt lgkmcnt(0)
	v_fmac_f32_e32 v24, v176, v58
	v_pk_fma_f32 v[10:11], v[178:179], v[30:31], v[10:11] op_sel_hi:[0,1,1]
	v_pk_fma_f32 v[12:13], v[178:179], v[38:39], v[12:13] op_sel_hi:[0,1,1]
	v_pk_fma_f32 v[14:15], v[178:179], v[46:47], v[14:15] op_sel_hi:[0,1,1]
	v_pk_fma_f32 v[16:17], v[178:179], v[54:55], v[16:17] op_sel_hi:[0,1,1]
	v_fmac_f32_e32 v24, v178, v59
	v_pk_fma_f32 v[10:11], v[180:181], v[26:27], v[10:11] op_sel_hi:[0,1,1]
	v_pk_fma_f32 v[12:13], v[180:181], v[34:35], v[12:13] op_sel_hi:[0,1,1]
	v_pk_fma_f32 v[14:15], v[180:181], v[42:43], v[14:15] op_sel_hi:[0,1,1]
	v_pk_fma_f32 v[16:17], v[180:181], v[50:51], v[16:17] op_sel_hi:[0,1,1]
	v_fmac_f32_e32 v24, v180, v60
	v_pk_fma_f32 v[10:11], v[182:183], v[32:33], v[10:11] op_sel_hi:[0,1,1]
	v_pk_fma_f32 v[12:13], v[182:183], v[40:41], v[12:13] op_sel_hi:[0,1,1]
	v_pk_fma_f32 v[14:15], v[182:183], v[48:49], v[14:15] op_sel_hi:[0,1,1]
	v_pk_fma_f32 v[16:17], v[182:183], v[56:57], v[16:17] op_sel_hi:[0,1,1]
	v_fmac_f32_e32 v24, v182, v61
	v_add_u32_e32 v25, s11, v19
	v_add_u32_e32 v26, 0x11000, v25
	v_add_u32_e32 v30, 0x12000, v25
	v_add_u32_e32 v34, 0x13000, v25
	v_add_u32_e32 v38, 0x14000, v25
	v_add_u32_e32 v42, 0x15000, v25
	v_add_u32_e32 v46, 0x16000, v25
	v_add_u32_e32 v50, 0x17000, v25
	v_add_u32_e32 v54, 0x18000, v25
	v_add_u32_e32 v25, 0x19000, v25
	ds_read_b128 v[26:29], v26 offset:224
	ds_read_b128 v[30:33], v30 offset:224
	ds_read_b128 v[34:37], v34 offset:224
	ds_read_b128 v[38:41], v38 offset:224
	ds_read_b128 v[42:45], v42 offset:224
	ds_read_b128 v[46:49], v46 offset:224
	ds_read_b128 v[50:53], v50 offset:224
	ds_read_b128 v[54:57], v54 offset:224
	ds_read_b128 v[58:61], v25 offset:224
	s_waitcnt lgkmcnt(8)
	v_mov_b32_e32 v70, v26
	s_waitcnt lgkmcnt(7)
	v_mov_b32_e32 v71, v30
	v_mov_b32_e32 v30, v27
	v_mov_b32_e32 v26, v28
	v_mov_b32_e32 v27, v32
	v_mov_b32_e32 v32, v29
	s_waitcnt lgkmcnt(6)
	v_mov_b32_e32 v28, v34
	s_waitcnt lgkmcnt(5)
	v_mov_b32_e32 v29, v38
	v_mov_b32_e32 v38, v35
	v_mov_b32_e32 v34, v36
	v_mov_b32_e32 v35, v40
	v_mov_b32_e32 v40, v37
	s_waitcnt lgkmcnt(4)
	v_mov_b32_e32 v36, v42
	s_waitcnt lgkmcnt(3)
	v_mov_b32_e32 v37, v46
	v_mov_b32_e32 v46, v43
	v_mov_b32_e32 v42, v44
	v_mov_b32_e32 v43, v48
	v_mov_b32_e32 v48, v45
	s_waitcnt lgkmcnt(2)
	v_mov_b32_e32 v44, v50
	s_waitcnt lgkmcnt(1)
	v_mov_b32_e32 v45, v54
	v_mov_b32_e32 v54, v51
	v_mov_b32_e32 v50, v52
	v_mov_b32_e32 v51, v56
	v_mov_b32_e32 v56, v53
	s_waitcnt vmcnt(36)
	v_pk_fma_f32 v[10:11], v[184:185], v[70:71], v[10:11] op_sel_hi:[0,1,1]
	v_pk_fma_f32 v[12:13], v[184:185], v[28:29], v[12:13] op_sel_hi:[0,1,1]
	v_pk_fma_f32 v[14:15], v[184:185], v[36:37], v[14:15] op_sel_hi:[0,1,1]
	v_pk_fma_f32 v[16:17], v[184:185], v[44:45], v[16:17] op_sel_hi:[0,1,1]
	s_waitcnt lgkmcnt(0)
	v_fmac_f32_e32 v24, v184, v58
	v_pk_fma_f32 v[10:11], v[186:187], v[30:31], v[10:11] op_sel_hi:[0,1,1]
	v_pk_fma_f32 v[12:13], v[186:187], v[38:39], v[12:13] op_sel_hi:[0,1,1]
	v_pk_fma_f32 v[14:15], v[186:187], v[46:47], v[14:15] op_sel_hi:[0,1,1]
	v_pk_fma_f32 v[16:17], v[186:187], v[54:55], v[16:17] op_sel_hi:[0,1,1]
	v_fmac_f32_e32 v24, v186, v59
	v_pk_fma_f32 v[10:11], v[188:189], v[26:27], v[10:11] op_sel_hi:[0,1,1]
	v_pk_fma_f32 v[12:13], v[188:189], v[34:35], v[12:13] op_sel_hi:[0,1,1]
	v_pk_fma_f32 v[14:15], v[188:189], v[42:43], v[14:15] op_sel_hi:[0,1,1]
	v_pk_fma_f32 v[16:17], v[188:189], v[50:51], v[16:17] op_sel_hi:[0,1,1]
	v_fmac_f32_e32 v24, v188, v60
	v_pk_fma_f32 v[10:11], v[190:191], v[32:33], v[10:11] op_sel_hi:[0,1,1]
	v_pk_fma_f32 v[12:13], v[190:191], v[40:41], v[12:13] op_sel_hi:[0,1,1]
	v_pk_fma_f32 v[14:15], v[190:191], v[48:49], v[14:15] op_sel_hi:[0,1,1]
	v_pk_fma_f32 v[16:17], v[190:191], v[56:57], v[16:17] op_sel_hi:[0,1,1]
	v_fmac_f32_e32 v24, v190, v61
	v_add_u32_e32 v25, s11, v19
	v_add_u32_e32 v26, 0x11000, v25
	v_add_u32_e32 v30, 0x12000, v25
	v_add_u32_e32 v34, 0x13000, v25
	v_add_u32_e32 v38, 0x14000, v25
	v_add_u32_e32 v42, 0x15000, v25
	v_add_u32_e32 v46, 0x16000, v25
	v_add_u32_e32 v50, 0x17000, v25
	v_add_u32_e32 v54, 0x18000, v25
	v_add_u32_e32 v25, 0x19000, v25
	ds_read_b128 v[26:29], v26 offset:240
	ds_read_b128 v[30:33], v30 offset:240
	ds_read_b128 v[34:37], v34 offset:240
	ds_read_b128 v[38:41], v38 offset:240
	ds_read_b128 v[42:45], v42 offset:240
	ds_read_b128 v[46:49], v46 offset:240
	ds_read_b128 v[50:53], v50 offset:240
	ds_read_b128 v[54:57], v54 offset:240
	ds_read_b128 v[58:61], v25 offset:240
	s_waitcnt lgkmcnt(8)
	v_mov_b32_e32 v70, v26
	s_waitcnt lgkmcnt(7)
	v_mov_b32_e32 v71, v30
	v_mov_b32_e32 v30, v27
	v_mov_b32_e32 v26, v28
	v_mov_b32_e32 v27, v32
	v_mov_b32_e32 v32, v29
	s_waitcnt lgkmcnt(6)
	v_mov_b32_e32 v28, v34
	s_waitcnt lgkmcnt(5)
	v_mov_b32_e32 v29, v38
	v_mov_b32_e32 v38, v35
	v_mov_b32_e32 v34, v36
	v_mov_b32_e32 v35, v40
	v_mov_b32_e32 v40, v37
	s_waitcnt lgkmcnt(4)
	v_mov_b32_e32 v36, v42
	s_waitcnt lgkmcnt(3)
	v_mov_b32_e32 v37, v46
	v_mov_b32_e32 v46, v43
	v_mov_b32_e32 v42, v44
	v_mov_b32_e32 v43, v48
	v_mov_b32_e32 v48, v45
	s_waitcnt lgkmcnt(2)
	v_mov_b32_e32 v44, v50
	s_waitcnt lgkmcnt(1)
	v_mov_b32_e32 v45, v54
	v_mov_b32_e32 v54, v51
	v_mov_b32_e32 v50, v52
	v_mov_b32_e32 v51, v56
	v_mov_b32_e32 v56, v53
	s_waitcnt vmcnt(32)
	v_pk_fma_f32 v[10:11], v[192:193], v[70:71], v[10:11] op_sel_hi:[0,1,1]
	v_pk_fma_f32 v[12:13], v[192:193], v[28:29], v[12:13] op_sel_hi:[0,1,1]
	v_pk_fma_f32 v[14:15], v[192:193], v[36:37], v[14:15] op_sel_hi:[0,1,1]
	v_pk_fma_f32 v[16:17], v[192:193], v[44:45], v[16:17] op_sel_hi:[0,1,1]
	s_waitcnt lgkmcnt(0)
	v_fmac_f32_e32 v24, v192, v58
	v_pk_fma_f32 v[10:11], v[194:195], v[30:31], v[10:11] op_sel_hi:[0,1,1]
	v_pk_fma_f32 v[12:13], v[194:195], v[38:39], v[12:13] op_sel_hi:[0,1,1]
	v_pk_fma_f32 v[14:15], v[194:195], v[46:47], v[14:15] op_sel_hi:[0,1,1]
	v_pk_fma_f32 v[16:17], v[194:195], v[54:55], v[16:17] op_sel_hi:[0,1,1]
	v_fmac_f32_e32 v24, v194, v59
	v_pk_fma_f32 v[10:11], v[196:197], v[26:27], v[10:11] op_sel_hi:[0,1,1]
	v_pk_fma_f32 v[12:13], v[196:197], v[34:35], v[12:13] op_sel_hi:[0,1,1]
	v_pk_fma_f32 v[14:15], v[196:197], v[42:43], v[14:15] op_sel_hi:[0,1,1]
	v_pk_fma_f32 v[16:17], v[196:197], v[50:51], v[16:17] op_sel_hi:[0,1,1]
	v_fmac_f32_e32 v24, v196, v60
	v_pk_fma_f32 v[10:11], v[198:199], v[32:33], v[10:11] op_sel_hi:[0,1,1]
	v_pk_fma_f32 v[12:13], v[198:199], v[40:41], v[12:13] op_sel_hi:[0,1,1]
	v_pk_fma_f32 v[14:15], v[198:199], v[48:49], v[14:15] op_sel_hi:[0,1,1]
	v_pk_fma_f32 v[16:17], v[198:199], v[56:57], v[16:17] op_sel_hi:[0,1,1]
	v_fmac_f32_e32 v24, v198, v61
	global_load_dword v136, v[8:9], off
	v_lshl_add_u64 v[8:9], v[8:9], 0, s[8:9]
	global_load_dword v138, v[8:9], off
	v_lshl_add_u64 v[8:9], v[8:9], 0, s[8:9]
	global_load_dword v140, v[8:9], off
	v_lshl_add_u64 v[8:9], v[8:9], 0, s[8:9]
	global_load_dword v142, v[8:9], off
	v_lshl_add_u64 v[8:9], v[8:9], 0, s[8:9]
	global_load_dword v144, v[8:9], off
	v_lshl_add_u64 v[8:9], v[8:9], 0, s[8:9]
	global_load_dword v146, v[8:9], off
	v_lshl_add_u64 v[8:9], v[8:9], 0, s[8:9]
	global_load_dword v148, v[8:9], off
	v_lshl_add_u64 v[8:9], v[8:9], 0, s[8:9]
	global_load_dword v150, v[8:9], off
	v_lshl_add_u64 v[8:9], v[8:9], 0, s[8:9]
	global_load_dword v152, v[8:9], off
	v_lshl_add_u64 v[8:9], v[8:9], 0, s[8:9]
	global_load_dword v154, v[8:9], off
	v_lshl_add_u64 v[8:9], v[8:9], 0, s[8:9]
	global_load_dword v156, v[8:9], off
	v_lshl_add_u64 v[8:9], v[8:9], 0, s[8:9]
	global_load_dword v158, v[8:9], off
	v_lshl_add_u64 v[8:9], v[8:9], 0, s[8:9]
	global_load_dword v160, v[8:9], off
	v_lshl_add_u64 v[8:9], v[8:9], 0, s[8:9]
	global_load_dword v162, v[8:9], off
	v_lshl_add_u64 v[8:9], v[8:9], 0, s[8:9]
	global_load_dword v164, v[8:9], off
	v_lshl_add_u64 v[8:9], v[8:9], 0, s[8:9]
	global_load_dword v166, v[8:9], off
	v_lshl_add_u64 v[8:9], v[8:9], 0, s[8:9]
	global_load_dword v168, v[8:9], off
	v_lshl_add_u64 v[8:9], v[8:9], 0, s[8:9]
	global_load_dword v170, v[8:9], off
	v_lshl_add_u64 v[8:9], v[8:9], 0, s[8:9]
	global_load_dword v172, v[8:9], off
	v_lshl_add_u64 v[8:9], v[8:9], 0, s[8:9]
	global_load_dword v174, v[8:9], off
	v_lshl_add_u64 v[8:9], v[8:9], 0, s[8:9]
	global_load_dword v176, v[8:9], off
	v_lshl_add_u64 v[8:9], v[8:9], 0, s[8:9]
	global_load_dword v178, v[8:9], off
	v_lshl_add_u64 v[8:9], v[8:9], 0, s[8:9]
	global_load_dword v180, v[8:9], off
	v_lshl_add_u64 v[8:9], v[8:9], 0, s[8:9]
	global_load_dword v182, v[8:9], off
	v_lshl_add_u64 v[8:9], v[8:9], 0, s[8:9]
	global_load_dword v184, v[8:9], off
	v_lshl_add_u64 v[8:9], v[8:9], 0, s[8:9]
	global_load_dword v186, v[8:9], off
	v_lshl_add_u64 v[8:9], v[8:9], 0, s[8:9]
	global_load_dword v188, v[8:9], off
	v_lshl_add_u64 v[8:9], v[8:9], 0, s[8:9]
	global_load_dword v190, v[8:9], off
	v_lshl_add_u64 v[8:9], v[8:9], 0, s[8:9]
	global_load_dword v192, v[8:9], off
	v_lshl_add_u64 v[8:9], v[8:9], 0, s[8:9]
	global_load_dword v194, v[8:9], off
	v_lshl_add_u64 v[8:9], v[8:9], 0, s[8:9]
	global_load_dword v196, v[8:9], off
	v_lshl_add_u64 v[8:9], v[8:9], 0, s[8:9]
	global_load_dword v198, v[8:9], off
	v_lshl_add_u64 v[8:9], v[8:9], 0, s[8:9]
	s_addk_i32 s11, 0x100
	s_cmpk_lg_i32 s11, 0x400
	s_cbranch_scc1 .Lmod_loop
	s_waitcnt vmcnt(0)
	ds_write2st64_b32 v23, v10, v11 offset1:2
	ds_write2st64_b32 v23, v12, v13 offset0:4 offset1:6
	ds_write2st64_b32 v23, v14, v15 offset0:8 offset1:10
	ds_write2st64_b32 v23, v16, v17 offset0:12 offset1:14
	ds_write_b32 v23, v24 offset:4096
	s_waitcnt lgkmcnt(0)
	s_barrier
	s_and_saveexec_b64 s[2:3], s[0:1]
	s_cbranch_execz .LBB0_16
	v_mov_b32_e32 v8, s15
	ds_read_b64 v[8:9], v8
	s_mul_i32 s11, s10, 0x1800
	v_add_u32_e32 v10, s11, v4
	s_mul_i32 s21, s10, 9
	v_ashrrev_i32_e32 v11, 31, v10
	v_lshl_add_u64 v[4:5], v[4:5], 2, s[4:5]
	s_mov_b64 s[10:11], 0
	v_mov_b32_e32 v12, v20
	v_mov_b32_e32 v13, v6

	.amdhsa_kernel _Z4mega4Args
		.amdhsa_group_segment_fixed_size 0
		.amdhsa_private_segment_fixed_size 0
		.amdhsa_kernarg_size 512
		.amdhsa_user_sgpr_count 2
		.amdhsa_user_sgpr_dispatch_ptr 0
		.amdhsa_user_sgpr_queue_ptr 0
		.amdhsa_user_sgpr_kernarg_segment_ptr 1
		.amdhsa_user_sgpr_dispatch_id 0
		.amdhsa_user_sgpr_kernarg_preload_length 0
		.amdhsa_user_sgpr_kernarg_preload_offset 0
		.amdhsa_user_sgpr_private_segment_size 0
		.amdhsa_uses_dynamic_stack 0
		.amdhsa_enable_private_segment 0
		.amdhsa_system_sgpr_workgroup_id_x 1
		.amdhsa_system_sgpr_workgroup_id_y 0
		.amdhsa_system_sgpr_workgroup_id_z 0
		.amdhsa_system_sgpr_workgroup_info 0
		.amdhsa_system_vgpr_workitem_id 0
		.amdhsa_next_free_vgpr 244
		.amdhsa_next_free_sgpr 102
		.amdhsa_accum_offset 244
		.amdhsa_reserve_vcc 1
		.amdhsa_float_round_mode_32 0
		.amdhsa_float_round_mode_16_64 0
		.amdhsa_float_denorm_mode_32 3
		.amdhsa_float_denorm_mode_16_64 3
		.amdhsa_dx10_clamp 1
		.amdhsa_ieee_mode 1
		.amdhsa_fp16_overflow 0
		.amdhsa_tg_split 0
		.amdhsa_exception_fp_ieee_invalid_op 0
		.amdhsa_exception_fp_denorm_src 0
		.amdhsa_exception_fp_ieee_div_zero 0
		.amdhsa_exception_fp_ieee_overflow 0
		.amdhsa_exception_fp_ieee_underflow 0
		.amdhsa_exception_fp_ieee_inexact 0
		.amdhsa_exception_int_div_zero 0
	.end_amdhsa_kernel

amdhsa.kernels:
  - .agpr_count:     0
    .args:
      - .offset:         0
        .size:           256
        .value_kind:     by_value
      - .offset:         256
        .size:           4
        .value_kind:     hidden_block_count_x
      - .offset:         260
        .size:           4
        .value_kind:     hidden_block_count_y
      - .offset:         264
        .size:           4
        .value_kind:     hidden_block_count_z
      - .offset:         268
        .size:           2
        .value_kind:     hidden_group_size_x
      - .offset:         270
        .size:           2
        .value_kind:     hidden_group_size_y
      - .offset:         272
        .size:           2
        .value_kind:     hidden_group_size_z
      - .offset:         274
        .size:           2
        .value_kind:     hidden_remainder_x
      - .offset:         276
        .size:           2
        .value_kind:     hidden_remainder_y
      - .offset:         278
        .size:           2
        .value_kind:     hidden_remainder_z
      - .offset:         296
        .size:           8
        .value_kind:     hidden_global_offset_x
      - .offset:         304
        .size:           8
        .value_kind:     hidden_global_offset_y
      - .offset:         312
        .size:           8
        .value_kind:     hidden_global_offset_z
      - .offset:         320
        .size:           2
        .value_kind:     hidden_grid_dims
      - .offset:         376
        .size:           4
        .value_kind:     hidden_dynamic_lds_size
    .group_segment_fixed_size: 0
    .kernarg_segment_align: 8
    .kernarg_segment_size: 512
    .language:       OpenCL C
    .language_version:
      - 2
      - 0
    .max_flat_workgroup_size: 512
    .name:           _Z4mega4Args
    .private_segment_fixed_size: 0
    .sgpr_count:     108
    .sgpr_spill_count: 386
    .symbol:         _Z4mega4Args.kd
    .uniform_work_group_size: 1
    .uses_dynamic_stack: false
    .vgpr_count:     244
    .vgpr_spill_count: 0
    .wavefront_size: 64
